# MoE scatter loop software-pipelined: the next step's assignment words and row scales are requested together with this step's row loads (one exposed round trip per step instead of two)
# speedup vs baseline: 1.0007x; 1.0007x over previous
.Lsc_top:
	v_readfirstlane_b32 s41, v32
	s_nop 0
	s_ashr_i32 s26, s41, 24
	s_cmp_eq_u32 s26, 1
	s_cselect_b32 s27, s6, 0
	s_cmp_eq_u32 s26, 2
	s_cselect_b32 s27, s7, s27
	s_cmp_eq_u32 s26, 3
	s_cselect_b32 s27, s30, s27
	s_cmp_eq_u32 s26, 4
	s_cselect_b32 s27, s31, s27
	s_cmp_eq_u32 s26, 5
	s_cselect_b32 s27, s33, s27
	s_cmp_eq_u32 s26, 6
	s_cselect_b32 s27, s34, s27
	s_cmp_eq_u32 s26, 7
	s_cselect_b32 s26, s35, s27
	s_and_b32 s27, s41, 0xffffff
	s_add_i32 s12, s26, s27
	v_mov_b32_e32 v32, s40
	s_ashr_i32 s10, s40, 1
	s_ashr_i32 s11, s10, 31
	s_lshl_b64 s[10:11], s[10:11], 10
	v_lshl_add_u64 v[2:3], v[20:21], 0, s[10:11]
	global_load_dwordx4 v[44:47], v[2:3], off
	s_cmp_eq_u32 s44, 0
	s_cbranch_scc1 .Lsc_rw1
	v_readfirstlane_b32 s41, v34
	s_nop 0
	s_ashr_i32 s26, s41, 24
	s_cmp_eq_u32 s26, 1
	s_cselect_b32 s27, s6, 0
	s_cmp_eq_u32 s26, 2
	s_cselect_b32 s27, s7, s27
	s_cmp_eq_u32 s26, 3
	s_cselect_b32 s27, s30, s27
	s_cmp_eq_u32 s26, 4
	s_cselect_b32 s27, s31, s27
	s_cmp_eq_u32 s26, 5
	s_cselect_b32 s27, s33, s27
	s_cmp_eq_u32 s26, 6
	s_cselect_b32 s27, s34, s27
	s_cmp_eq_u32 s26, 7
	s_cselect_b32 s26, s35, s27
	s_and_b32 s27, s41, 0xffffff
	s_add_i32 s13, s26, s27
	v_mov_b32_e32 v34, s20
	s_ashr_i32 s10, s20, 1
	s_ashr_i32 s11, s10, 31
	s_lshl_b64 s[10:11], s[10:11], 10
	v_lshl_add_u64 v[2:3], v[20:21], 0, s[10:11]
	global_load_dwordx4 v[48:51], v[2:3], off

.Lsc_rw3:
	s_add_i32 s41, s40, s52
	s_mul_i32 s26, s46, 24
	s_add_i32 s26, s26, s41
	s_cmp_lt_i32 s26, 0x10000
	s_cbranch_scc0 .Lsc_nopf
	s_mov_b32 s26, s41
	s_ashr_i32 s10, s26, 1
	s_ashr_i32 s11, s10, 31
	s_lshl_b64 s[10:11], s[10:11], 2
	s_add_u32 s10, s36, s10
	s_addc_u32 s11, s37, s11
	global_load_dword v68, v1, s[10:11]
	s_add_u32 s10, s18, s62
	s_addc_u32 s11, s19, s63
	global_load_dwordx2 v[60:61], v1, s[10:11]
	s_add_i32 s26, s42, s41
	s_ashr_i32 s10, s26, 1
	s_ashr_i32 s11, s10, 31
	s_lshl_b64 s[10:11], s[10:11], 2
	s_add_u32 s10, s36, s10
	s_addc_u32 s11, s37, s11
	global_load_dword v69, v1, s[10:11]
	s_ashr_i32 s11, s26, 31
	s_mov_b32 s10, s26
	s_lshl_b64 s[10:11], s[10:11], 3
	s_add_u32 s10, s4, s10
	s_addc_u32 s11, s5, s11
	global_load_dwordx2 v[62:63], v1, s[10:11]
	s_add_i32 s26, s65, s41
	s_ashr_i32 s10, s26, 1
	s_ashr_i32 s11, s10, 31
	s_lshl_b64 s[10:11], s[10:11], 2
	s_add_u32 s10, s36, s10
	s_addc_u32 s11, s37, s11
	global_load_dword v70, v1, s[10:11]
	s_ashr_i32 s11, s26, 31
	s_mov_b32 s10, s26
	s_lshl_b64 s[10:11], s[10:11], 3
	s_add_u32 s10, s4, s10
	s_addc_u32 s11, s5, s11
	global_load_dwordx2 v[64:65], v1, s[10:11]
	s_mul_i32 s26, s46, 24
	s_add_i32 s26, s26, s41
	s_ashr_i32 s10, s26, 1
	s_ashr_i32 s11, s10, 31
	s_lshl_b64 s[10:11], s[10:11], 2
	s_add_u32 s10, s36, s10
	s_addc_u32 s11, s37, s11
	global_load_dword v71, v1, s[10:11]
	s_ashr_i32 s11, s26, 31
	s_mov_b32 s10, s26
	s_lshl_b64 s[10:11], s[10:11], 3
	s_add_u32 s10, s4, s10
	s_addc_u32 s11, s5, s11
	global_load_dwordx2 v[66:67], v1, s[10:11]
	s_mov_b32 s41, 1
	s_waitcnt vmcnt(8)
	s_branch .Lsc_p3
.Lsc_nopf:
	s_mov_b32 s41, 0
	s_waitcnt vmcnt(0)
.Lsc_p3:
	s_mov_b32 s26, s12
	s_mov_b32 s27, 0
	s_lshl_b64 s[10:11], s[26:27], 3
	s_add_u32 s10, s16, s10
	s_addc_u32 s11, s17, s11
	s_lshl_b64 s[28:29], s[26:27], 2
	s_add_u32 s28, s38, s28
	s_addc_u32 s29, s39, s29
	s_lshl_b64 s[26:27], s[26:27], 10
	v_lshl_add_u64 v[2:3], v[22:23], 0, s[26:27]
	s_and_saveexec_b64 s[26:27], s[8:9]
	global_store_dwordx2 v1, v[32:33], s[10:11]
	global_store_dword v1, v40, s[28:29]
	s_or_b64 exec, exec, s[26:27]
	global_store_dwordx4 v[2:3], v[44:47], off
	s_cmp_eq_u32 s44, 0
	s_cbranch_scc1 .Lsc_st1
	s_mov_b32 s26, s13
	s_mov_b32 s27, 0
	s_lshl_b64 s[10:11], s[26:27], 3
	s_add_u32 s10, s16, s10
	s_addc_u32 s11, s17, s11
	s_lshl_b64 s[28:29], s[26:27], 2
	s_add_u32 s28, s38, s28
	s_addc_u32 s29, s39, s29
	s_lshl_b64 s[26:27], s[26:27], 10
	v_lshl_add_u64 v[2:3], v[22:23], 0, s[26:27]
	s_and_saveexec_b64 s[26:27], s[8:9]
	global_store_dwordx2 v1, v[34:35], s[10:11]
	global_store_dword v1, v41, s[28:29]
	s_or_b64 exec, exec, s[26:27]
	global_store_dwordx4 v[2:3], v[48:51], off

.Lsc_st3:
	s_add_i32 s40, s40, s52
	s_add_u32 s18, s18, s62
	s_addc_u32 s19, s19, s63
	s_cmp_eq_u32 s41, 1
	s_cbranch_scc1 .Lsc_pfnext
	s_cmp_lt_i32 s40, 0x10000
	s_cbranch_scc1 .LBB0_1085
	s_branch .Lsc_exit
.Lsc_pfnext:
	s_cmp_eq_u32 s48, 1
	s_cbranch_scc1 .Lsc_w12
	s_waitcnt vmcnt(0)
	s_branch .Lsc_cp
.Lsc_w12:
	s_waitcnt vmcnt(12)
.Lsc_cp:
	v_mov_b32_e32 v32, v60
	v_mov_b32_e32 v33, v61
	v_mov_b32_e32 v40, v68
	v_mov_b32_e32 v34, v62
	v_mov_b32_e32 v35, v63
	v_mov_b32_e32 v41, v69
	v_mov_b32_e32 v36, v64
	v_mov_b32_e32 v37, v65
	v_mov_b32_e32 v42, v70
	v_mov_b32_e32 v38, v66
	v_mov_b32_e32 v39, v67
	v_mov_b32_e32 v43, v71
	s_add_i32 s20, s42, s40
	s_add_i32 s24, s65, s40
	s_mul_i32 s22, s46, 24
	s_add_i32 s22, s22, s40
	s_mov_b32 s44, 1
	s_mov_b32 s45, 1
	s_mov_b32 s48, 1
	s_branch .Lsc_top
.Lsc_exit:
.LBB0_1114:
	s_mov_b64 s[70:71], s[54:55]
	s_mov_b32 s4, s58
	s_waitcnt vmcnt(0)
	s_barrier
	s_mov_b64 s[6:7], exec
	v_readlane_b32 s8, v252, 2
	v_readlane_b32 s9, v252, 3
	s_and_b64 s[8:9], s[6:7], s[8:9]
	s_xor_b64 s[40:41], s[8:9], s[6:7]
	s_mov_b64 exec, s[8:9]
	s_cbranch_execz .LBB0_1159
	v_readlane_b32 s5, v254, 58
	s_waitcnt vmcnt(0) expcnt(0) lgkmcnt(0)
	s_nop 0
	v_mov_b32_e32 v0, s5
	ds_read_b32 v2, v0
	v_readlane_b32 s5, v254, 59
	s_waitcnt lgkmcnt(0)
	v_cmp_ne_u32_e32 vcc, 0, v2
	v_mov_b32_e32 v0, s5
	ds_read_b32 v0, v0
	s_cbranch_vccnz .LBB0_1129
	v_readlane_b32 s8, v252, 0
	v_readlane_b32 s9, v252, 1
	s_load_dwordx2 s[6:7], s[8:9], 0x4
	s_add_u32 s8, s70, 0x1000
	s_addc_u32 s9, s71, 0
	s_add_u32 s10, s70, 0x1100
	s_addc_u32 s11, s71, 0
	s_add_u32 s12, s70, 0x1200
	s_addc_u32 s13, s71, 0
	s_waitcnt lgkmcnt(0)
	s_mul_i32 s5, s6, s46
	s_add_u32 s14, s70, 0x1300
	s_mul_i32 s5, s5, s7
	s_addc_u32 s15, s71, 0
	s_mov_b32 s6, 1
	s_mov_b64 s[16:17], 0
	s_branch .LBB0_1119
